# P4: waves 4-7 start half a unit late (stagger) so the two waves of a SIMD do not stall on their prefetch packing waits together
# baseline (speedup 1.0000x reference)
; #define GAS __attribute__((address_space(1)))
; #define LAS __attribute__((address_space(3)))
; __global__ void __launch_bounds__(NTHR, 2) mk_fwd(Args args) {
;     ...
;                 if (gw < 64 * NCHUNK) P4_FETCH(gw);
; #pragma unroll 1
;                 for (int u = gw; u < 64 * NCHUNK; u += NGW) {
;     ...
;                     { const v4u q_ = *(const LAS v4u*)(QGT + lane * 8), g_ = *(const LAS v4u*)(QGT + 512 + lane * 8), t_ = *(const LAS v4u*)(QGT + 1024 + lane * 8);
;                       *(GAS v4u*)(pk + PK_QQ + lane * 16) = q_; *(GAS v4u*)(pk + PK_GG + lane * 16) = g_; *(GAS v4u*)(pk + PK_TT + lane * 16) = t_; }
.LBB0_475:
	s_or_b64 exec, exec, s[34:35]
	s_waitcnt lgkmcnt(0)
	ds_read_b128 v[2:5], v125 offset:10240
	ds_read_b128 v[22:25], v125 offset:11264
	ds_read_b128 v[26:29], v125 offset:12288
	v_add_co_u32_e32 v20, vcc, 0x1000, v20
	s_add_i32 s48, s48, s51
	s_nop 0
	v_addc_co_u32_e32 v21, vcc, 0, v21, vcc
	s_waitcnt lgkmcnt(2)
	global_store_dwordx4 v[20:21], v[2:5], off
	s_waitcnt lgkmcnt(1)
	global_store_dwordx4 v[20:21], v[22:25], off offset:2048
	s_waitcnt lgkmcnt(0)
	global_store_dwordx4 v[20:21], v[26:29], off offset:1024
	s_waitcnt lgkmcnt(0)
	s_andn2_b64 vcc, exec, s[68:69]
	s_waitcnt vmcnt(51)
	v_mov_b32_e32 v57, v160
	s_waitcnt vmcnt(49)
	v_mov_b32_e32 v60, v163
	s_waitcnt vmcnt(47)
	v_mov_b32_e32 v63, v166
	s_waitcnt vmcnt(45)
	v_mov_b32_e32 v66, v169
	s_waitcnt vmcnt(43)
	v_mov_b32_e32 v68, v171
	s_waitcnt vmcnt(41)
	v_mov_b32_e32 v70, v173
	s_waitcnt vmcnt(39)
	v_mov_b32_e32 v72, v175
	s_waitcnt vmcnt(37)
	v_mov_b32_e32 v74, v177
	s_waitcnt vmcnt(35)
	v_mov_b32_e32 v76, v179
	s_waitcnt vmcnt(33)
	v_mov_b32_e32 v78, v181
	s_waitcnt vmcnt(31)
	v_mov_b32_e32 v80, v183
	s_waitcnt vmcnt(29)
	v_mov_b32_e32 v82, v185
	s_waitcnt vmcnt(27)
	v_mov_b32_e32 v84, v187
	s_waitcnt vmcnt(25)
	v_mov_b32_e32 v86, v189
	s_waitcnt vmcnt(23)
	v_mov_b32_e32 v88, v191
	s_waitcnt vmcnt(21)
	v_mov_b32_e32 v90, v193
	v_mov_b32_e32 v58, v162
	v_mov_b32_e32 v62, v165
	v_mov_b32_e32 v65, v168
	v_mov_b32_e32 v67, v170
	v_mov_b32_e32 v69, v172
	v_mov_b32_e32 v71, v174
	v_mov_b32_e32 v73, v176
	v_mov_b32_e32 v75, v178
	v_mov_b32_e32 v77, v180
	v_mov_b32_e32 v79, v182
	v_mov_b32_e32 v81, v184
	v_mov_b32_e32 v83, v186
	v_mov_b32_e32 v85, v188
	v_mov_b32_e32 v87, v190
	v_mov_b32_e32 v89, v192
	v_mov_b32_e32 v91, v196
	v_mov_b32_e32 v20, v127
	v_mov_b32_e32 v23, v130
	v_mov_b32_e32 v41, v146
	v_mov_b32_e32 v21, v126
	v_mov_b32_e32 v22, v129
	v_mov_b32_e32 v26, v132
	v_mov_b32_e32 v30, v134
	v_mov_b32_e32 v31, v136
	v_mov_b32_e32 v34, v138
	v_mov_b32_e32 v35, v140
	v_mov_b32_e32 v37, v142
	v_mov_b32_e32 v39, v144
	v_mov_b32_e32 v44, v147
	v_mov_b32_e32 v46, v149
	v_mov_b32_e32 v48, v151
	v_mov_b32_e32 v50, v153
	v_mov_b32_e32 v52, v155
	v_mov_b32_e32 v54, v157
	v_mov_b32_e32 v56, v159
	v_mov_b32_e32 v61, v164
	v_mov_b32_e32 v24, v128
	v_mov_b32_e32 v25, v131
	v_mov_b32_e32 v27, v133
	v_mov_b32_e32 v29, v135
	v_mov_b32_e32 v32, v137
	v_mov_b32_e32 v33, v139
	v_mov_b32_e32 v36, v141
	v_mov_b32_e32 v38, v143
	v_mov_b32_e32 v43, v145
	v_mov_b32_e32 v45, v148
	v_mov_b32_e32 v47, v150
	v_mov_b32_e32 v49, v152
	v_mov_b32_e32 v51, v154
	v_mov_b32_e32 v53, v156
	v_mov_b32_e32 v55, v158
	v_mov_b32_e32 v59, v161
	v_mov_b32_e32 v64, v167
	s_waitcnt vmcnt(14)
	v_mov_b32_e32 v3, v203
	v_mov_b32_e32 v28, v202
	v_mov_b32_e32 v94, v201
	v_mov_b32_e32 v95, v200
	v_mov_b32_e32 v2, v199
	v_mov_b32_e32 v42, v198
	v_mov_b32_e32 v40, v197
	s_mov_b32 s34, s75
	v_mov_b32_e32 v212, v204
	v_mov_b32_e32 v213, v205
	v_mov_b32_e32 v214, v206
	v_mov_b32_e32 v215, v207
	v_mov_b32_e32 v92, v208
	v_mov_b32_e32 v93, v209
	v_mov_b32_e32 v96, v210
	v_mov_b32_e32 v97, v211
	s_cbranch_vccz .LBB0_480
	v_readlane_b32 s0, v252, 43
	s_nop 3
	s_cmp_lt_u32 s0, 4
	s_cbranch_scc1 .Lp4_nostagger
	s_sleep 127
.Lp4_nostagger:
.LBB0_476:
	s_add_i32 s75, s34, s28
	s_cmpk_gt_i32 s75, 0x3fff
	s_cselect_b64 s[68:69], -1, 0
	s_and_b64 vcc, exec, s[68:69]
	v_mov_b32_e32 v199, v2
	s_cbranch_vccnz .LBB0_478
	s_ashr_i32 s0, s75, 12
	s_bfe_u32 s40, s75, 0x80004
	s_ashr_i32 s1, s0, 31
	s_lshl_b64 s[0:1], s[0:1], 12
	s_lshl_b32 s35, s40, 4
	s_or_b32 s88, s0, s35
	s_add_u32 s43, s88, -1
	s_addc_u32 s64, s1, -1
	s_and_b32 s35, s48, 0x3c0
	s_lshl_b32 s76, s35, 1
	s_cmp_eq_u32 s40, 0
	v_lshl_add_u64 v[4:5], v[14:15], 0, s[76:77]
	s_cselect_b32 s0, s0, s43
	s_cselect_b32 s1, s1, s64
	s_mul_i32 s40, s1, 0x2400
	v_mad_u64_u32 v[130:131], s[0:1], s0, v99, v[4:5]
	v_add_u32_e32 v131, s40, v131
	global_load_ushort v128, v[130:131], off
	global_load_ushort v126, v[130:131], off offset:2048
	v_add_co_u32_e32 v130, vcc, s36, v130
	v_mad_i64_i32 v[4:5], s[0:1], s88, v99, v[4:5]
	s_nop 0
	v_addc_co_u32_e32 v131, vcc, 0, v131, vcc
	v_add_co_u32_e32 v132, vcc, s36, v4
	global_load_ushort v127, v[130:131], off
	s_nop 0
	v_addc_co_u32_e32 v133, vcc, 0, v5, vcc
	global_load_ushort v131, v[4:5], off
	global_load_ushort v129, v[4:5], off offset:2048
	global_load_ushort v130, v[132:133], off
	s_mov_b64 s[0:1], 0x2400
	v_add_co_u32_e32 v132, vcc, s37, v4
	v_lshl_add_u64 v[134:135], v[4:5], 0, s[0:1]
	s_nop 0
	v_addc_co_u32_e32 v133, vcc, 0, v5, vcc
	global_load_ushort v133, v[132:133], off offset:1024
	s_nop 0
	global_load_ushort v132, v[134:135], off offset:2048
	v_add_co_u32_e32 v134, vcc, s38, v4
	s_movk_i32 s40, 0x4000
	s_nop 0
	v_addc_co_u32_e32 v135, vcc, 0, v5, vcc
	global_load_ushort v207, v[134:135], off offset:1024
	s_mov_b64 s[64:65], 0x4800
	v_add_co_u32_e32 v134, vcc, s40, v4
	v_lshl_add_u64 v[136:137], v[4:5], 0, s[64:65]
	s_nop 0
	v_addc_co_u32_e32 v135, vcc, 0, v5, vcc
	s_movk_i32 s0, 0x5000
	global_load_ushort v135, v[134:135], off offset:2048
	s_nop 0
	global_load_ushort v134, v[136:137], off offset:2048
	v_add_co_u32_e32 v136, vcc, s0, v4
	s_movk_i32 s43, 0x6000
	s_nop 0
	v_addc_co_u32_e32 v137, vcc, 0, v5, vcc
	global_load_ushort v208, v[136:137], off offset:2048
	s_mov_b64 s[0:1], 0x6c00
	v_add_co_u32_e32 v136, vcc, s43, v4
	v_lshl_add_u64 v[138:139], v[4:5], 0, s[0:1]
	s_nop 0
	v_addc_co_u32_e32 v137, vcc, 0, v5, vcc
	global_load_ushort v137, v[136:137], off offset:3072
	s_nop 0
	global_load_ushort v136, v[138:139], off offset:2048
	v_add_co_u32_e32 v138, vcc, s42, v4
	s_mov_b64 s[70:71], 0x9000
	s_nop 0
	v_addc_co_u32_e32 v139, vcc, 0, v5, vcc
	v_add_co_u32_e32 v142, vcc, s44, v4
	s_mov_b64 s[0:1], 0xb400
	s_nop 0
	v_addc_co_u32_e32 v143, vcc, 0, v5, vcc
	global_load_ushort v206, v[138:139], off offset:3072
	v_lshl_add_u64 v[140:141], v[4:5], 0, s[70:71]
	global_load_ushort v139, v[142:143], off offset:-4096
	global_load_ushort v138, v[140:141], off offset:2048
	global_load_ushort v209, v[142:143], off
	v_lshl_add_u64 v[142:143], v[4:5], 0, s[0:1]
	s_mov_b32 s0, 0xb000
	v_add_co_u32_e32 v140, vcc, s0, v4
	s_mov_b64 s[80:81], 0xd800
	s_nop 0
	v_addc_co_u32_e32 v141, vcc, 0, v5, vcc
	global_load_ushort v141, v[140:141], off offset:1024
	s_nop 0
	global_load_ushort v140, v[142:143], off offset:2048
	v_add_co_u32_e32 v142, vcc, s39, v4
	v_lshl_add_u64 v[144:145], v[4:5], 0, s[80:81]
	s_nop 0
	v_addc_co_u32_e32 v143, vcc, 0, v5, vcc
	global_load_ushort v204, v[142:143], off offset:1024
	v_add_co_u32_e32 v142, vcc, s41, v4
	s_mov_b32 s0, 0xe000
	s_nop 0
	v_addc_co_u32_e32 v143, vcc, 0, v5, vcc
	global_load_ushort v143, v[142:143], off offset:2048
	s_nop 0
	global_load_ushort v142, v[144:145], off offset:2048
	v_add_co_u32_e32 v144, vcc, s0, v4
	s_mov_b64 s[0:1], 0xfc00
	s_nop 0
	v_addc_co_u32_e32 v145, vcc, 0, v5, vcc
	global_load_ushort v205, v[144:145], off offset:2048
	v_add_co_u32_e32 v144, vcc, s49, v4
	v_lshl_add_u64 v[146:147], v[4:5], 0, s[0:1]
	s_nop 0
	v_addc_co_u32_e32 v145, vcc, 0, v5, vcc
	global_load_ushort v145, v[144:145], off offset:3072
	s_nop 0
	global_load_ushort v144, v[146:147], off offset:2048
	v_add_co_u32_e32 v146, vcc, s50, v4
	s_mov_b64 s[0:1], 0x14400
	s_nop 0
	v_addc_co_u32_e32 v147, vcc, 0, v5, vcc
	v_add_co_u32_e32 v150, vcc, s73, v4
	global_load_ushort v210, v[146:147], off offset:3072
	v_lshl_add_u64 v[146:147], v[4:5], 0, s[46:47]
	v_addc_co_u32_e32 v151, vcc, 0, v5, vcc
	v_lshl_add_u64 v[152:153], v[4:5], 0, s[0:1]
	s_mov_b32 s0, 0x14000
	global_load_ushort v148, v[150:151], off offset:-4096
	s_nop 0
	global_load_ushort v147, v[146:147], off offset:2048
	s_nop 0
	global_load_ushort v146, v[150:151], off
	v_add_co_u32_e32 v150, vcc, s0, v4
	s_mov_b64 s[82:83], 0x16800
	s_nop 0
	v_addc_co_u32_e32 v151, vcc, 0, v5, vcc
	global_load_ushort v150, v[150:151], off offset:1024
	s_nop 0
	global_load_ushort v149, v[152:153], off offset:2048
	v_add_co_u32_e32 v152, vcc, s78, v4
	v_lshl_add_u64 v[154:155], v[4:5], 0, s[82:83]
	s_nop 0
	v_addc_co_u32_e32 v153, vcc, 0, v5, vcc
	global_load_ushort v211, v[152:153], off offset:1024
	v_add_co_u32_e32 v152, vcc, s72, v4
	s_mov_b32 s0, 0x17000
	s_nop 0
	v_addc_co_u32_e32 v153, vcc, 0, v5, vcc
	global_load_ushort v152, v[152:153], off offset:2048
	s_nop 0
	global_load_ushort v151, v[154:155], off offset:2048
	v_add_co_u32_e32 v154, vcc, s0, v4
	s_mov_b64 s[0:1], 0x18c00
	s_nop 0
	v_addc_co_u32_e32 v155, vcc, 0, v5, vcc
	v_lshl_add_u64 v[156:157], v[4:5], 0, s[0:1]
	s_mov_b32 s0, 0x18000
	global_load_ushort v216, v[154:155], off offset:2048
	v_add_co_u32_e32 v154, vcc, s0, v4
	s_mov_b32 s0, 0x19000
	s_nop 0
	v_addc_co_u32_e32 v155, vcc, 0, v5, vcc
	global_load_ushort v154, v[154:155], off offset:3072
	s_nop 0
	global_load_ushort v153, v[156:157], off offset:2048
	v_add_co_u32_e32 v156, vcc, s0, v4
	s_mov_b64 s[0:1], 0x1b000
	s_nop 0
	v_addc_co_u32_e32 v157, vcc, 0, v5, vcc
	v_lshl_add_u64 v[158:159], v[4:5], 0, s[0:1]
	s_mov_b32 s0, 0x1c000
	v_add_co_u32_e32 v160, vcc, s0, v4
	s_mov_b64 s[0:1], 0x1d400
	s_nop 0
	v_addc_co_u32_e32 v161, vcc, 0, v5, vcc
	global_load_ushort v217, v[156:157], off offset:3072
	s_nop 0
	global_load_ushort v156, v[160:161], off offset:-4096
	global_load_ushort v155, v[158:159], off offset:2048
	global_load_ushort v218, v[160:161], off
	v_lshl_add_u64 v[160:161], v[4:5], 0, s[0:1]
	s_mov_b32 s0, 0x1d000
	v_add_co_u32_e32 v158, vcc, s0, v4
	s_mov_b32 s0, 0x1e000
	s_nop 0
	v_addc_co_u32_e32 v159, vcc, 0, v5, vcc
	global_load_ushort v158, v[158:159], off offset:1024
	s_nop 0
	global_load_ushort v157, v[160:161], off offset:2048
	v_add_co_u32_e32 v160, vcc, s0, v4
	s_mov_b64 s[0:1], 0x1f800
	s_nop 0
	v_addc_co_u32_e32 v161, vcc, 0, v5, vcc
	v_lshl_add_u64 v[162:163], v[4:5], 0, s[0:1]
	s_mov_b32 s0, 0x1f000
	global_load_ushort v219, v[160:161], off offset:1024
	v_add_co_u32_e32 v160, vcc, s0, v4
	s_mov_b32 s0, 0x20000
	s_nop 0
	v_addc_co_u32_e32 v161, vcc, 0, v5, vcc
	global_load_ushort v161, v[160:161], off offset:2048
	s_nop 0
	global_load_ushort v159, v[162:163], off offset:2048
	v_add_co_u32_e32 v162, vcc, s0, v4
	s_mov_b64 s[0:1], 0x21c00
	s_nop 0
	v_addc_co_u32_e32 v163, vcc, 0, v5, vcc
	global_load_ushort v220, v[162:163], off offset:2048
	v_lshl_add_u64 v[162:163], v[4:5], 0, s[0:1]
	s_mov_b32 s0, 0x21000
	v_add_co_u32_e32 v164, vcc, s0, v4
	s_mov_b32 s0, 0x22000
	s_nop 0
	v_addc_co_u32_e32 v165, vcc, 0, v5, vcc
	v_add_co_u32_e32 v4, vcc, s0, v4
	global_load_ushort v167, v[164:165], off offset:3072
	s_nop 0
	global_load_ushort v164, v[162:163], off offset:2048
	v_addc_co_u32_e32 v5, vcc, 0, v5, vcc
	global_load_ushort v221, v[4:5], off offset:3072
	v_lshl_add_u64 v[4:5], v[16:17], 0, s[76:77]
	v_mad_i64_i32 v[4:5], s[0:1], s88, v100, v[4:5]
	s_mov_b64 s[0:1], 0x1800
	v_add_co_u32_e32 v170, vcc, s36, v4
	v_lshl_add_u64 v[168:169], v[4:5], 0, s[0:1]
	s_nop 0
	v_addc_co_u32_e32 v171, vcc, 0, v5, vcc
	global_load_ushort v162, v[4:5], off
	global_load_ushort v160, v[4:5], off offset:2048
	global_load_ushort v165, v[170:171], off offset:2048
	global_load_ushort v163, v[168:169], off offset:2048
	s_mov_b64 s[0:1], 0x3000
	v_add_co_u32_e32 v168, vcc, s38, v4
	v_lshl_add_u64 v[170:171], v[4:5], 0, s[0:1]
	s_nop 0
	v_addc_co_u32_e32 v169, vcc, 0, v5, vcc
	global_load_ushort v168, v[168:169], off
	s_nop 0
	global_load_ushort v166, v[170:171], off offset:2048
	v_add_co_u32_e32 v170, vcc, s40, v4
	v_lshl_add_u64 v[172:173], v[4:5], 0, s[64:65]
	s_nop 0
	v_addc_co_u32_e32 v171, vcc, 0, v5, vcc
	global_load_ushort v170, v[170:171], off offset:2048
	s_nop 0
	global_load_ushort v169, v[172:173], off offset:2048
	s_mov_b64 s[0:1], 0x6000
	v_add_co_u32_e32 v172, vcc, s43, v4
	v_lshl_add_u64 v[174:175], v[4:5], 0, s[0:1]
	s_nop 0
	v_addc_co_u32_e32 v173, vcc, 0, v5, vcc
	global_load_ushort v172, v[172:173], off
	s_nop 0
	global_load_ushort v171, v[174:175], off offset:2048
	s_mov_b64 s[0:1], 0x7800
	v_add_co_u32_e32 v174, vcc, s42, v4
	v_lshl_add_u64 v[176:177], v[4:5], 0, s[0:1]
	s_nop 0
	v_addc_co_u32_e32 v175, vcc, 0, v5, vcc
	s_mov_b32 s0, 0x9000
	global_load_ushort v174, v[174:175], off offset:2048
	s_nop 0
	global_load_ushort v173, v[176:177], off offset:2048
	v_add_co_u32_e32 v176, vcc, s0, v4
	v_lshl_add_u64 v[178:179], v[4:5], 0, s[70:71]
	s_nop 0
	v_addc_co_u32_e32 v177, vcc, 0, v5, vcc
	global_load_ushort v176, v[176:177], off
	s_nop 0
	global_load_ushort v175, v[178:179], off offset:2048
	s_mov_b64 s[0:1], 0xa800
	v_add_co_u32_e32 v178, vcc, s44, v4
	v_lshl_add_u64 v[180:181], v[4:5], 0, s[0:1]
	s_nop 0
	v_addc_co_u32_e32 v179, vcc, 0, v5, vcc
	global_load_ushort v178, v[178:179], off offset:2048
	s_nop 0
	global_load_ushort v177, v[180:181], off offset:2048
	s_mov_b64 s[0:1], 0xc000
	v_add_co_u32_e32 v180, vcc, s39, v4
	v_lshl_add_u64 v[182:183], v[4:5], 0, s[0:1]
	s_nop 0
	v_addc_co_u32_e32 v181, vcc, 0, v5, vcc
	global_load_ushort v180, v[180:181], off
	s_nop 0
	global_load_ushort v179, v[182:183], off offset:2048
	v_add_co_u32_e32 v182, vcc, s41, v4
	v_lshl_add_u64 v[184:185], v[4:5], 0, s[80:81]
	s_nop 0
	v_addc_co_u32_e32 v183, vcc, 0, v5, vcc
	global_load_ushort v182, v[182:183], off offset:2048
	s_nop 0
	global_load_ushort v181, v[184:185], off offset:2048
	s_mov_b64 s[0:1], 0xf000
	v_add_co_u32_e32 v184, vcc, s49, v4
	v_lshl_add_u64 v[186:187], v[4:5], 0, s[0:1]
	s_nop 0
	v_addc_co_u32_e32 v185, vcc, 0, v5, vcc
	global_load_ushort v184, v[184:185], off
	s_nop 0
	global_load_ushort v183, v[186:187], off offset:2048
	s_mov_b64 s[0:1], 0x10800
	v_add_co_u32_e32 v186, vcc, s50, v4
	v_lshl_add_u64 v[188:189], v[4:5], 0, s[0:1]
	s_nop 0
	v_addc_co_u32_e32 v187, vcc, 0, v5, vcc
	s_mov_b32 s0, 0x12000
	global_load_ushort v186, v[186:187], off offset:2048
	s_nop 0
	global_load_ushort v185, v[188:189], off offset:2048
	v_add_co_u32_e32 v188, vcc, s0, v4
	v_lshl_add_u64 v[190:191], v[4:5], 0, s[46:47]
	s_nop 0
	v_addc_co_u32_e32 v189, vcc, 0, v5, vcc
	global_load_ushort v188, v[188:189], off
	s_nop 0
	global_load_ushort v187, v[190:191], off offset:2048
	s_mov_b64 s[0:1], 0x13800
	v_add_co_u32_e32 v190, vcc, s73, v4
	v_lshl_add_u64 v[192:193], v[4:5], 0, s[0:1]
	s_nop 0
	v_addc_co_u32_e32 v191, vcc, 0, v5, vcc
	global_load_ushort v190, v[190:191], off offset:2048
	s_nop 0
	global_load_ushort v189, v[192:193], off offset:2048
	v_add_co_u32_e32 v192, vcc, s78, v4
	s_mov_b64 s[0:1], 0x15000
	s_nop 0
	v_addc_co_u32_e32 v193, vcc, 0, v5, vcc
	v_lshl_add_u64 v[196:197], v[4:5], 0, s[0:1]
	v_lshl_add_u64 v[198:199], v[4:5], 0, s[82:83]
	v_add_co_u32_e32 v4, vcc, s72, v4
	global_load_ushort v192, v[192:193], off
	s_nop 0
	global_load_ushort v191, v[196:197], off offset:2048
	v_addc_co_u32_e32 v5, vcc, 0, v5, vcc
	global_load_ushort v196, v[4:5], off offset:2048
	global_load_ushort v193, v[198:199], off offset:2048
	v_or_b32_e32 v4, s35, v194
	v_readlane_b32 s80, v252, 0
	v_lshlrev_b32_e32 v4, 2, v4
	v_mov_b32_e32 v5, v7
	v_readlane_b32 s84, v252, 4
	v_readlane_b32 s85, v252, 5
	v_readlane_b32 s86, v252, 6
	v_readlane_b32 s87, v252, 7
	v_lshl_add_u64 v[200:201], s[84:85], 0, v[4:5]
	v_add_co_u32_e32 v198, vcc, s36, v200
	v_readlane_b32 s90, v252, 10
	s_nop 0
	v_addc_co_u32_e32 v199, vcc, 0, v201, vcc
	v_add_co_u32_e32 v200, vcc, 0x2000, v200
	v_readlane_b32 s91, v252, 11
	s_nop 0
	v_addc_co_u32_e32 v201, vcc, 0, v201, vcc
	global_load_dword v197, v4, s[84:85]
	s_waitcnt vmcnt(60)
	v_perm_b32 v204, v205, v204, s45
	global_load_dword v198, v[198:199], off
	s_nop 0
	global_load_dword v199, v[200:201], off
	s_nop 0
	global_load_dword v200, v4, s[86:87]
	global_load_dword v201, v4, s[90:91]
	global_load_dword v202, v4, s[52:53]
	global_load_dword v203, v4, s[54:55]
	s_waitcnt vmcnt(62)
	v_perm_b32 v205, v210, v205, s45
	v_perm_b32 v206, v209, v206, s45
	v_perm_b32 v207, v208, v207, s45
	s_waitcnt vmcnt(42)
	v_perm_b32 v208, v220, v219, s45
	s_waitcnt vmcnt(39)
	v_perm_b32 v209, v221, v220, s45
	v_perm_b32 v210, v218, v217, s45
	v_perm_b32 v211, v216, v211, s45
	v_readlane_b32 s81, v252, 1
	v_readlane_b32 s82, v252, 2
	v_readlane_b32 s83, v252, 3
	v_readlane_b32 s88, v252, 8
	v_readlane_b32 s89, v252, 9
	v_readlane_b32 s92, v252, 12
	v_readlane_b32 s93, v252, 13
	v_readlane_b32 s94, v252, 14
	v_readlane_b32 s95, v252, 15
